# speedup vs baseline: 1.0196x; 1.0082x over previous
.LBB1_135:
	v_mov_b32_e32 v32, 0xff800000
	v_cmp_neq_f32_e32 vcc, 0, v80
	s_nop 1
	v_cndmask_b32_e32 v80, v32, v80, vcc
	v_cmp_neq_f32_e32 vcc, 0, v96
	s_nop 1
	v_cndmask_b32_e32 v96, v32, v96, vcc
	v_cmp_neq_f32_e32 vcc, 0, v81
	s_nop 1
	v_cndmask_b32_e32 v81, v32, v81, vcc
	v_cmp_neq_f32_e32 vcc, 0, v97
	s_nop 1
	v_cndmask_b32_e32 v97, v32, v97, vcc
	v_cmp_neq_f32_e32 vcc, 0, v82
	s_nop 1
	v_cndmask_b32_e32 v82, v32, v82, vcc
	v_cmp_neq_f32_e32 vcc, 0, v98
	s_nop 1
	v_cndmask_b32_e32 v98, v32, v98, vcc
	v_cmp_neq_f32_e32 vcc, 0, v83
	s_nop 1
	v_cndmask_b32_e32 v83, v32, v83, vcc
	v_cmp_neq_f32_e32 vcc, 0, v99
	s_nop 1
	v_cndmask_b32_e32 v99, v32, v99, vcc
	v_cmp_neq_f32_e32 vcc, 0, v84
	s_nop 1
	v_cndmask_b32_e32 v84, v32, v84, vcc
	v_cmp_neq_f32_e32 vcc, 0, v100
	s_nop 1
	v_cndmask_b32_e32 v100, v32, v100, vcc
	v_cmp_neq_f32_e32 vcc, 0, v85
	s_nop 1
	v_cndmask_b32_e32 v85, v32, v85, vcc
	v_cmp_neq_f32_e32 vcc, 0, v101
	s_nop 1
	v_cndmask_b32_e32 v101, v32, v101, vcc
	v_cmp_neq_f32_e32 vcc, 0, v86
	s_nop 1
	v_cndmask_b32_e32 v86, v32, v86, vcc
	v_cmp_neq_f32_e32 vcc, 0, v102
	s_nop 1
	v_cndmask_b32_e32 v102, v32, v102, vcc
	v_cmp_neq_f32_e32 vcc, 0, v87
	s_nop 1
	v_cndmask_b32_e32 v87, v32, v87, vcc
	v_cmp_neq_f32_e32 vcc, 0, v103
	s_nop 1
	v_cndmask_b32_e32 v103, v32, v103, vcc
	v_cmp_neq_f32_e32 vcc, 0, v88
	s_nop 1
	v_cndmask_b32_e32 v88, v32, v88, vcc
	v_cmp_neq_f32_e32 vcc, 0, v104
	s_nop 1
	v_cndmask_b32_e32 v104, v32, v104, vcc
	v_cmp_neq_f32_e32 vcc, 0, v89
	s_nop 1
	v_cndmask_b32_e32 v89, v32, v89, vcc
	v_cmp_neq_f32_e32 vcc, 0, v105
	s_nop 1
	v_cndmask_b32_e32 v105, v32, v105, vcc
	v_cmp_neq_f32_e32 vcc, 0, v90
	s_nop 1
	v_cndmask_b32_e32 v90, v32, v90, vcc
	v_cmp_neq_f32_e32 vcc, 0, v106
	s_nop 1
	v_cndmask_b32_e32 v106, v32, v106, vcc
	v_cmp_neq_f32_e32 vcc, 0, v91
	s_nop 1
	v_cndmask_b32_e32 v91, v32, v91, vcc
	v_cmp_neq_f32_e32 vcc, 0, v107
	s_nop 1
	v_cndmask_b32_e32 v107, v32, v107, vcc
	v_cmp_neq_f32_e32 vcc, 0, v92
	s_nop 1
	v_cndmask_b32_e32 v92, v32, v92, vcc
	v_cmp_neq_f32_e32 vcc, 0, v108
	s_nop 1
	v_cndmask_b32_e32 v108, v32, v108, vcc
	v_cmp_neq_f32_e32 vcc, 0, v93
	s_nop 1
	v_cndmask_b32_e32 v93, v32, v93, vcc
	v_cmp_neq_f32_e32 vcc, 0, v109
	s_nop 1
	v_cndmask_b32_e32 v109, v32, v109, vcc
	v_cmp_neq_f32_e32 vcc, 0, v94
	s_nop 1
	v_cndmask_b32_e32 v94, v32, v94, vcc
	v_cmp_neq_f32_e32 vcc, 0, v110
	s_nop 1
	v_cndmask_b32_e32 v110, v32, v110, vcc
	v_cmp_neq_f32_e32 vcc, 0, v95
	s_nop 1
	v_cndmask_b32_e32 v95, v32, v95, vcc
	v_cmp_neq_f32_e32 vcc, 0, v111
	s_nop 1
	v_cndmask_b32_e32 v111, v32, v111, vcc
	s_branch .LBB1_93
	s_nop 0
	s_nop 0
	s_nop 0
	s_nop 0
	s_nop 0
	s_nop 0
	s_nop 0
	s_nop 0
	s_nop 0
	s_nop 0
	s_nop 0
	s_nop 0
	s_nop 0
	s_nop 0
	s_nop 0
	s_nop 0
	s_nop 0
	s_nop 0
	s_nop 0
	s_nop 0
	s_nop 0
	s_nop 0
	s_nop 0
	s_nop 0
	s_nop 0
	s_nop 0
	s_nop 0
	s_nop 0
	s_endpgm
